# G1 K-loop: LDS-DMA loads use SGPR base + 32-bit VGPR offset (scalar adds for the K-step bases) instead of a v_lshl_add_u64 per load
# speedup vs baseline: 1.0028x; 1.0010x over previous
; #define PG8_STAGE(bufoff, gbase, voff) do { _Pragma("unroll") for (int _i = 0; _i < 2; ++_i) \
;         __builtin_amdgcn_global_load_lds((const unsigned*)((const char*)(gbase) + (voff)[_i]), (PG8_LAS unsigned*)(lds + (bufoff) + ldsw + _i * 8192), 16, 0, 0); } while (0)
; #define PG8_LDA(dst, b, h) do { _Pragma("unroll") for (int m = 0; m < 4; ++m) _Pragma("unroll") for (int k = 0; k < 2; ++k) dst[m][k] = *(const PG8_LAS bf16x8*)(lds + PG8_SA(b, h) + aoff + m * 2048 + k * 1024); } while (0)
; #define PG8_LDB(dst, b, h) do { _Pragma("unroll") for (int n = 0; n < 2; ++n) _Pragma("unroll") for (int k = 0; k < 2; ++k) dst[n][k] = *(const PG8_LAS bf16x8*)(lds + PG8_SB(b, h) + boff + n * 2048 + k * 1024); } while (0)
; #define PG8_WAIT_V(n) asm volatile("s_waitcnt vmcnt(" #n ")" ::: "memory")
; #define PG8_WAIT_L(n) asm volatile("s_waitcnt lgkmcnt(" #n ")" ::: "memory")
; #define PG8_BAR __builtin_amdgcn_s_barrier()
; #define PG8_SCHED __builtin_amdgcn_sched_barrier(0)
; template <class Epi, class Sched, bool ALIGN_EPI = false, bool SP2 = false>
; __device__ __forceinline__ void gemm_phase(PG8_LAS unsigned char* lds, const Gemm g, const Sched& S, const Epi& E, const int tid) {
;     ...
;         const bool has_next = S.next(ui + 1, nxt);
;         const char* nA = has_next ? (const char*)g.A + (size_t)nxt.pm * tstep : cA; const char* nB = has_next ? (const char*)g.Bt + (size_t)nxt.pn * tstep : cB;
;         for (int t = 0; t < nt; t += 2) {
;             const bool last = (t == nt - 2);
;             const char* a1 = cA + (size_t)(t + 1) * kstep;
;             const char* a2 = last ? nA : cA + (size_t)(t + 2) * kstep; const char* b2 = last ? nB : cB + (size_t)(t + 2) * kstep;
;             const char* a3 = a2 + kstep; const char* b3 = b2 + kstep;
;             if (last && has_next) S.a_ready(nxt);
;             if constexpr (SP2) {
;             PG8_LDB(B0, 0, 0); PG8_LDB(B1, 0, 1); PG8_SCHED; PG8_LDA(At, 0, 0); PG8_STAGE(PG8_SA(1, 1), a1 + hstep, voffA);
;             PG8_WAIT_V(8); PG8_WAIT_L(0); PG8_BAR; PG8_MMA(0, 0, At, B0); PG8_MMA(0, 1, At, B1); PG8_BAR; PG8_SCHED;
;             PG8_LDA(At, 0, 1); PG8_STAGE(PG8_SB(0, 0), b2, voffB); PG8_STAGE(PG8_SB(0, 1), b2, voffB1); PG8_STAGE(PG8_SA(0, 0), a2, voffA);
;             PG8_WAIT_V(8); PG8_WAIT_L(0); PG8_BAR; PG8_MMA(1, 0, At, B0); PG8_MMA(1, 1, At, B1); PG8_BAR; PG8_SCHED;
.LBB0_726:
	s_ashr_i32 s11, s10, 31
	s_lshl_b64 s[12:13], s[10:11], 19
	s_add_u32 s12, s38, s12
	s_addc_u32 s13, s39, s13
	s_and_b64 s[14:15], s[2:3], exec
	s_cselect_b32 s11, s13, s47
	s_cselect_b32 s59, s12, s46
	s_ashr_i32 s9, s8, 31
	s_lshl_b64 s[14:15], s[8:9], 19
	s_add_u32 s14, s40, s14
	s_addc_u32 s15, s41, s15
	s_and_b64 s[36:37], s[2:3], exec
	s_cselect_b32 s9, s15, s53
	s_cselect_b32 s60, s14, s52
	s_add_u32 s46, s46, 0x40080
	s_addc_u32 s47, s47, 0
	s_add_u32 s52, s52, 0x100
	s_addc_u32 s53, s53, 0
	s_mov_b32 s62, -2
	s_add_u32 s36, s46, 0xfffc0080
	s_addc_u32 s37, s47, -1
	s_add_i32 s63, 0, 0x10000
	s_cmp_eq_u32 s62, 12
	s_cselect_b32 s37, s11, s37
	s_cselect_b32 s36, s59, s36
	v_add_u32_e32 v148, s63, v151
	s_cselect_b32 s73, s9, s53
	s_cselect_b32 s72, s60, s52
	s_add_i32 s68, 0, 0x14000
	ds_read_b128 v[144:147], v148
	ds_read_b128 v[156:159], v148 offset:1024
	ds_read_b128 v[160:163], v148 offset:2048
	ds_read_b128 v[164:167], v148 offset:3072
	v_add_u32_e32 v148, s68, v151
	ds_read_b128 v[168:171], v148
	ds_read_b128 v[172:175], v148 offset:1024
	ds_read_b128 v[176:179], v148 offset:2048
	ds_read_b128 v[180:183], v148 offset:3072
	s_add_i32 m0, s43, 0xc000
	ds_read_b128 v[184:187], v154
	ds_read_b128 v[188:191], v154 offset:1024
	ds_read_b128 v[192:195], v154 offset:2048
	ds_read_b128 v[196:199], v154 offset:3072
	ds_read_b128 v[212:215], v154 offset:4096
	ds_read_b128 v[216:219], v154 offset:5120
	ds_read_b128 v[220:223], v154 offset:6144
	ds_read_b128 v[224:227], v154 offset:7168
	global_load_lds_dwordx4 v140, s[46:47]
	s_add_i32 m0, s43, 0xe000
	s_nop 0
	global_load_lds_dwordx4 v142, s[46:47]
	s_waitcnt vmcnt(8)
	s_waitcnt lgkmcnt(0)
	s_barrier
	s_setprio 1
	s_waitcnt lgkmcnt(0)
	v_mfma_f32_16x16x32_bf16 v[128:131], v[144:147], v[184:187], 0
	v_mfma_f32_16x16x32_bf16 v[120:123], v[160:163], v[184:187], 0
	v_mfma_f32_16x16x32_bf16 v[112:115], v[144:147], v[192:195], 0
	v_mfma_f32_16x16x32_bf16 v[104:107], v[160:163], v[192:195], 0
	v_mfma_f32_16x16x32_bf16 v[96:99], v[144:147], v[212:215], 0
	v_mfma_f32_16x16x32_bf16 v[88:91], v[160:163], v[212:215], 0
	v_mfma_f32_16x16x32_bf16 v[80:83], v[144:147], v[220:223], 0
	v_mfma_f32_16x16x32_bf16 v[72:75], v[160:163], v[220:223], 0
	v_mfma_f32_16x16x32_bf16 v[128:131], v[156:159], v[188:191], v[128:131]
	v_mfma_f32_16x16x32_bf16 v[120:123], v[164:167], v[188:191], v[120:123]
	v_mfma_f32_16x16x32_bf16 v[112:115], v[156:159], v[196:199], v[112:115]
	v_mfma_f32_16x16x32_bf16 v[104:107], v[164:167], v[196:199], v[104:107]
	v_mfma_f32_16x16x32_bf16 v[96:99], v[156:159], v[216:219], v[96:99]
	v_mfma_f32_16x16x32_bf16 v[88:91], v[164:167], v[216:219], v[88:91]
	v_mfma_f32_16x16x32_bf16 v[80:83], v[156:159], v[224:227], v[80:83]
	v_mfma_f32_16x16x32_bf16 v[72:75], v[164:167], v[224:227], v[72:75]
	s_setprio 0
	s_setprio 1
	v_mfma_f32_16x16x32_bf16 v[124:127], v[168:171], v[184:187], 0
	v_mfma_f32_16x16x32_bf16 v[116:119], v[176:179], v[184:187], 0
	v_mfma_f32_16x16x32_bf16 v[108:111], v[168:171], v[192:195], 0
	v_mfma_f32_16x16x32_bf16 v[100:103], v[176:179], v[192:195], 0
	v_mfma_f32_16x16x32_bf16 v[92:95], v[168:171], v[212:215], 0
	v_mfma_f32_16x16x32_bf16 v[84:87], v[176:179], v[212:215], 0
	v_mfma_f32_16x16x32_bf16 v[76:79], v[168:171], v[220:223], 0
	v_mfma_f32_16x16x32_bf16 v[68:71], v[176:179], v[220:223], 0
	v_mfma_f32_16x16x32_bf16 v[124:127], v[172:175], v[188:191], v[124:127]
	v_mfma_f32_16x16x32_bf16 v[116:119], v[180:183], v[188:191], v[116:119]
	v_mfma_f32_16x16x32_bf16 v[108:111], v[172:175], v[196:199], v[108:111]
	v_mfma_f32_16x16x32_bf16 v[100:103], v[180:183], v[196:199], v[100:103]
	v_mfma_f32_16x16x32_bf16 v[92:95], v[172:175], v[216:219], v[92:95]
	v_mfma_f32_16x16x32_bf16 v[84:87], v[180:183], v[216:219], v[84:87]
	v_mfma_f32_16x16x32_bf16 v[76:79], v[172:175], v[224:227], v[76:79]
	v_mfma_f32_16x16x32_bf16 v[68:71], v[180:183], v[224:227], v[68:71]
	s_setprio 0
	s_barrier
	s_add_i32 s63, s63, s33
	s_mov_b32 m0, s63
	ds_read_b128 v[184:187], v154 offset:16384
	ds_read_b128 v[188:191], v154 offset:17408
	ds_read_b128 v[192:195], v154 offset:18432
	ds_read_b128 v[196:199], v154 offset:19456
	ds_read_b128 v[212:215], v154 offset:20480
	ds_read_b128 v[216:219], v154 offset:21504
	ds_read_b128 v[220:223], v154 offset:22528
	ds_read_b128 v[224:227], v154 offset:23552
	global_load_lds_dwordx4 v2, s[72:73]
	s_add_i32 m0, s63, 0x2000
	s_add_i32 s63, s68, s33
	global_load_lds_dwordx4 v132, s[72:73]
	s_mov_b32 m0, s63
	s_nop 0
	global_load_lds_dwordx4 v136, s[72:73]
	s_add_i32 m0, s63, 0x2000
	s_nop 0
	global_load_lds_dwordx4 v0, s[72:73]
	s_mov_b32 m0, s43
	s_nop 0
	global_load_lds_dwordx4 v138, s[36:37]
	s_mov_b32 m0, s45
	s_nop 0
	global_load_lds_dwordx4 v134, s[36:37]
	s_waitcnt vmcnt(8)
	s_waitcnt lgkmcnt(0)
	s_barrier
; #define PG8_STAGE(bufoff, gbase, voff) do { _Pragma("unroll") for (int _i = 0; _i < 2; ++_i) \
;         __builtin_amdgcn_global_load_lds((const unsigned*)((const char*)(gbase) + (voff)[_i]), (PG8_LAS unsigned*)(lds + (bufoff) + ldsw + _i * 8192), 16, 0, 0); } while (0)
; #define PG8_LDA(dst, b, h) do { _Pragma("unroll") for (int m = 0; m < 4; ++m) _Pragma("unroll") for (int k = 0; k < 2; ++k) dst[m][k] = *(const PG8_LAS bf16x8*)(lds + PG8_SA(b, h) + aoff + m * 2048 + k * 1024); } while (0)
; #define PG8_LDB(dst, b, h) do { _Pragma("unroll") for (int n = 0; n < 2; ++n) _Pragma("unroll") for (int k = 0; k < 2; ++k) dst[n][k] = *(const PG8_LAS bf16x8*)(lds + PG8_SB(b, h) + boff + n * 2048 + k * 1024); } while (0)
; #define PG8_MMA(ai, bj, At, Bt) do { __builtin_amdgcn_s_setprio(1); _Pragma("unroll") for (int m = 0; m < 4; ++m) _Pragma("unroll") for (int n = 0; n < 2; ++n) _Pragma("unroll") for (int k = 0; k < 2; ++k) \
;         acc[ai][bj][m][n] = __builtin_amdgcn_mfma_f32_16x16x32_bf16(Bt[n][k], At[m][k], acc[ai][bj][m][n], 0, 0, 0); __builtin_amdgcn_s_setprio(0); } while (0)
; #define PG8_WAIT_V(n) asm volatile("s_waitcnt vmcnt(" #n ")" ::: "memory")
; #define PG8_WAIT_L(n) asm volatile("s_waitcnt lgkmcnt(" #n ")" ::: "memory")
; #define PG8_BAR __builtin_amdgcn_s_barrier()
; #define PG8_SCHED __builtin_amdgcn_sched_barrier(0)
; template <class Epi, class Sched, bool ALIGN_EPI = false, bool SP2 = false>
; __device__ __forceinline__ void gemm_phase(PG8_LAS unsigned char* lds, const Gemm g, const Sched& S, const Epi& E, const int tid) {
;     ...
;             PG8_WAIT_V(8); PG8_WAIT_L(0); PG8_BAR; PG8_MMA(1, 0, At, B0); PG8_MMA(1, 1, At, B1); PG8_BAR; PG8_SCHED;
;             PG8_LDB(B0, 1, 0); PG8_LDB(B1, 1, 1); PG8_SCHED; PG8_LDA(At, 1, 0); PG8_STAGE(PG8_SA(0, 1), a2 + hstep, voffA);
;             PG8_WAIT_V(8); PG8_WAIT_L(0); PG8_BAR; PG8_MMA(0, 0, At, B0); PG8_MMA(0, 1, At, B1); PG8_BAR; PG8_SCHED;
	s_setprio 1
	s_waitcnt lgkmcnt(0)
	v_mfma_f32_16x16x32_bf16 v[64:67], v[144:147], v[184:187], 0
	v_mfma_f32_16x16x32_bf16 v[56:59], v[160:163], v[184:187], 0
	v_mfma_f32_16x16x32_bf16 v[48:51], v[144:147], v[192:195], 0
	v_mfma_f32_16x16x32_bf16 v[40:43], v[160:163], v[192:195], 0
	v_mfma_f32_16x16x32_bf16 v[32:35], v[144:147], v[212:215], 0
	v_mfma_f32_16x16x32_bf16 v[24:27], v[160:163], v[212:215], 0
	v_mfma_f32_16x16x32_bf16 v[16:19], v[144:147], v[220:223], 0
	v_mfma_f32_16x16x32_bf16 v[8:11], v[160:163], v[220:223], 0
	v_mfma_f32_16x16x32_bf16 v[64:67], v[156:159], v[188:191], v[64:67]
	v_mfma_f32_16x16x32_bf16 v[56:59], v[164:167], v[188:191], v[56:59]
	v_mfma_f32_16x16x32_bf16 v[48:51], v[156:159], v[196:199], v[48:51]
	v_mfma_f32_16x16x32_bf16 v[40:43], v[164:167], v[196:199], v[40:43]
	v_mfma_f32_16x16x32_bf16 v[32:35], v[156:159], v[216:219], v[32:35]
	v_mfma_f32_16x16x32_bf16 v[24:27], v[164:167], v[216:219], v[24:27]
	v_mfma_f32_16x16x32_bf16 v[16:19], v[156:159], v[224:227], v[16:19]
	v_mfma_f32_16x16x32_bf16 v[8:11], v[164:167], v[224:227], v[8:11]
	s_setprio 0
	s_setprio 1
	v_mfma_f32_16x16x32_bf16 v[60:63], v[168:171], v[184:187], 0
	v_mfma_f32_16x16x32_bf16 v[52:55], v[176:179], v[184:187], 0
	v_mfma_f32_16x16x32_bf16 v[44:47], v[168:171], v[192:195], 0
	v_mfma_f32_16x16x32_bf16 v[36:39], v[176:179], v[192:195], 0
	v_mfma_f32_16x16x32_bf16 v[28:31], v[168:171], v[212:215], 0
	v_mfma_f32_16x16x32_bf16 v[20:23], v[176:179], v[212:215], 0
	v_mfma_f32_16x16x32_bf16 v[12:15], v[168:171], v[220:223], 0
	v_mfma_f32_16x16x32_bf16 v[4:7], v[176:179], v[220:223], 0
	v_mfma_f32_16x16x32_bf16 v[60:63], v[172:175], v[188:191], v[60:63]
	v_mfma_f32_16x16x32_bf16 v[52:55], v[180:183], v[188:191], v[52:55]
	v_mfma_f32_16x16x32_bf16 v[44:47], v[172:175], v[196:199], v[44:47]
	v_mfma_f32_16x16x32_bf16 v[36:39], v[180:183], v[196:199], v[36:39]
	v_mfma_f32_16x16x32_bf16 v[28:31], v[172:175], v[216:219], v[28:31]
	v_mfma_f32_16x16x32_bf16 v[20:23], v[180:183], v[216:219], v[20:23]
	v_mfma_f32_16x16x32_bf16 v[12:15], v[172:175], v[224:227], v[12:15]
	v_mfma_f32_16x16x32_bf16 v[4:7], v[180:183], v[224:227], v[4:7]
	s_setprio 0
	s_barrier
	s_add_i32 s63, 0, 0x18000
	v_add_u32_e32 v155, s63, v151
	s_add_i32 s68, 0, 0x1c000
	ds_read_b128 v[144:147], v155
	ds_read_b128 v[156:159], v155 offset:1024
	ds_read_b128 v[160:163], v155 offset:2048
	ds_read_b128 v[164:167], v155 offset:3072
	v_add_u32_e32 v155, s68, v151
	ds_read_b128 v[168:171], v155
	ds_read_b128 v[172:175], v155 offset:1024
	ds_read_b128 v[176:179], v155 offset:2048
	ds_read_b128 v[180:183], v155 offset:3072
	s_add_u32 s36, s36, 0x40000
	s_addc_u32 s37, s37, 0
	s_mov_b32 m0, s48
	ds_read_b128 v[184:187], v154 offset:32768
	ds_read_b128 v[188:191], v154 offset:33792
	ds_read_b128 v[192:195], v154 offset:34816
	ds_read_b128 v[196:199], v154 offset:35840
	ds_read_b128 v[212:215], v154 offset:36864
	ds_read_b128 v[216:219], v154 offset:37888
	ds_read_b128 v[220:223], v154 offset:38912
	ds_read_b128 v[224:227], v154 offset:39936
	global_load_lds_dwordx4 v138, s[36:37]
	s_mov_b32 m0, s49
	s_nop 0
	global_load_lds_dwordx4 v134, s[36:37]
	s_waitcnt vmcnt(8)
	s_waitcnt lgkmcnt(0)
	s_barrier
	s_setprio 1
	s_waitcnt lgkmcnt(0)
	v_mfma_f32_16x16x32_bf16 v[128:131], v[144:147], v[184:187], v[128:131]
	v_mfma_f32_16x16x32_bf16 v[120:123], v[160:163], v[184:187], v[120:123]
	v_mfma_f32_16x16x32_bf16 v[112:115], v[144:147], v[192:195], v[112:115]
	v_mfma_f32_16x16x32_bf16 v[104:107], v[160:163], v[192:195], v[104:107]
	v_mfma_f32_16x16x32_bf16 v[96:99], v[144:147], v[212:215], v[96:99]
	v_mfma_f32_16x16x32_bf16 v[88:91], v[160:163], v[212:215], v[88:91]
	v_mfma_f32_16x16x32_bf16 v[80:83], v[144:147], v[220:223], v[80:83]
	v_mfma_f32_16x16x32_bf16 v[72:75], v[160:163], v[220:223], v[72:75]
	v_mfma_f32_16x16x32_bf16 v[128:131], v[156:159], v[188:191], v[128:131]
	v_mfma_f32_16x16x32_bf16 v[120:123], v[164:167], v[188:191], v[120:123]
	v_mfma_f32_16x16x32_bf16 v[112:115], v[156:159], v[196:199], v[112:115]
	v_mfma_f32_16x16x32_bf16 v[104:107], v[164:167], v[196:199], v[104:107]
	v_mfma_f32_16x16x32_bf16 v[96:99], v[156:159], v[216:219], v[96:99]
	v_mfma_f32_16x16x32_bf16 v[88:91], v[164:167], v[216:219], v[88:91]
	v_mfma_f32_16x16x32_bf16 v[80:83], v[156:159], v[224:227], v[80:83]
	v_mfma_f32_16x16x32_bf16 v[72:75], v[164:167], v[224:227], v[72:75]
	s_setprio 0
	s_setprio 1
	v_mfma_f32_16x16x32_bf16 v[124:127], v[168:171], v[184:187], v[124:127]
	v_mfma_f32_16x16x32_bf16 v[116:119], v[176:179], v[184:187], v[116:119]
	v_mfma_f32_16x16x32_bf16 v[108:111], v[168:171], v[192:195], v[108:111]
	v_mfma_f32_16x16x32_bf16 v[100:103], v[176:179], v[192:195], v[100:103]
	v_mfma_f32_16x16x32_bf16 v[92:95], v[168:171], v[212:215], v[92:95]
	v_mfma_f32_16x16x32_bf16 v[84:87], v[176:179], v[212:215], v[84:87]
	v_mfma_f32_16x16x32_bf16 v[76:79], v[168:171], v[220:223], v[76:79]
	v_mfma_f32_16x16x32_bf16 v[68:71], v[176:179], v[220:223], v[68:71]
	v_mfma_f32_16x16x32_bf16 v[124:127], v[172:175], v[188:191], v[124:127]
	v_mfma_f32_16x16x32_bf16 v[116:119], v[180:183], v[188:191], v[116:119]
	v_mfma_f32_16x16x32_bf16 v[108:111], v[172:175], v[196:199], v[108:111]
	v_mfma_f32_16x16x32_bf16 v[100:103], v[180:183], v[196:199], v[100:103]
	v_mfma_f32_16x16x32_bf16 v[92:95], v[172:175], v[216:219], v[92:95]
	v_mfma_f32_16x16x32_bf16 v[84:87], v[180:183], v[216:219], v[84:87]
	v_mfma_f32_16x16x32_bf16 v[76:79], v[172:175], v[224:227], v[76:79]
	v_mfma_f32_16x16x32_bf16 v[68:71], v[180:183], v[224:227], v[68:71]
	s_setprio 0
	s_barrier
; #define PG8_STAGE(bufoff, gbase, voff) do { _Pragma("unroll") for (int _i = 0; _i < 2; ++_i) \
;         __builtin_amdgcn_global_load_lds((const unsigned*)((const char*)(gbase) + (voff)[_i]), (PG8_LAS unsigned*)(lds + (bufoff) + ldsw + _i * 8192), 16, 0, 0); } while (0)
; #define PG8_LDA(dst, b, h) do { _Pragma("unroll") for (int m = 0; m < 4; ++m) _Pragma("unroll") for (int k = 0; k < 2; ++k) dst[m][k] = *(const PG8_LAS bf16x8*)(lds + PG8_SA(b, h) + aoff + m * 2048 + k * 1024); } while (0)
; #define PG8_LDB(dst, b, h) do { _Pragma("unroll") for (int n = 0; n < 2; ++n) _Pragma("unroll") for (int k = 0; k < 2; ++k) dst[n][k] = *(const PG8_LAS bf16x8*)(lds + PG8_SB(b, h) + boff + n * 2048 + k * 1024); } while (0)
; template <class Epi, class Sched, bool ALIGN_EPI = false, bool SP2 = false>
; __device__ __forceinline__ void gemm_phase(PG8_LAS unsigned char* lds, const Gemm g, const Sched& S, const Epi& E, const int tid) {
;     ...
;         for (int t = 0; t < nt; t += 2) {
;             const bool last = (t == nt - 2);
;             const char* a1 = cA + (size_t)(t + 1) * kstep;
;             const char* a2 = last ? nA : cA + (size_t)(t + 2) * kstep; const char* b2 = last ? nB : cB + (size_t)(t + 2) * kstep;
;             const char* a3 = a2 + kstep; const char* b3 = b2 + kstep;
;             if (last && has_next) S.a_ready(nxt);
;             if constexpr (SP2) {
;             PG8_LDB(B0, 0, 0); PG8_LDB(B1, 0, 1); PG8_SCHED; PG8_LDA(At, 0, 0); PG8_STAGE(PG8_SA(1, 1), a1 + hstep, voffA);
;             PG8_WAIT_V(8); PG8_WAIT_L(0); PG8_BAR; PG8_MMA(0, 0, At, B0); PG8_MMA(0, 1, At, B1); PG8_BAR; PG8_SCHED;
;             PG8_LDA(At, 0, 1); PG8_STAGE(PG8_SB(0, 0), b2, voffB); PG8_STAGE(PG8_SB(0, 1), b2, voffB1); PG8_STAGE(PG8_SA(0, 0), a2, voffA);
;             PG8_WAIT_V(8); PG8_WAIT_L(0); PG8_BAR; PG8_MMA(1, 0, At, B0); PG8_MMA(1, 1, At, B1); PG8_BAR; PG8_SCHED;
;             PG8_LDB(B0, 1, 0); PG8_LDB(B1, 1, 1); PG8_SCHED; PG8_LDA(At, 1, 0); PG8_STAGE(PG8_SA(0, 1), a2 + hstep, voffA);
;             PG8_WAIT_V(8); PG8_WAIT_L(0); PG8_BAR; PG8_MMA(0, 0, At, B0); PG8_MMA(0, 1, At, B1); PG8_BAR; PG8_SCHED;
;             PG8_LDA(At, 1, 1); PG8_STAGE(PG8_SB(1, 0), b3, voffB); PG8_STAGE(PG8_SB(1, 1), b3, voffB1); PG8_STAGE(PG8_SA(1, 0), a3, voffA);
;             PG8_WAIT_V(8); PG8_WAIT_L(0); PG8_BAR; PG8_MMA(1, 0, At, B0); PG8_MMA(1, 1, At, B1); PG8_BAR; PG8_SCHED;
	s_add_u32 s98, s36, s66
	s_addc_u32 s99, s37, s67
	s_sub_u32 s98, s98, 0x40000
	s_subb_u32 s99, s99, 0
	s_mov_b32 m0, s50
	ds_read_b128 v[184:187], v154 offset:49152
	ds_read_b128 v[188:191], v154 offset:50176
	ds_read_b128 v[192:195], v154 offset:51200
	ds_read_b128 v[196:199], v154 offset:52224
	ds_read_b128 v[212:215], v154 offset:53248
	ds_read_b128 v[216:219], v154 offset:54272
	ds_read_b128 v[220:223], v154 offset:55296
	ds_read_b128 v[224:227], v154 offset:56320
	global_load_lds_dwordx4 v138, s[98:99]
	s_mov_b32 m0, s51
	s_nop 0
	global_load_lds_dwordx4 v134, s[98:99]
	s_add_u32 s98, s72, s66
	s_addc_u32 s99, s73, s67
	s_add_i32 s36, s63, s33
	s_mov_b32 m0, s36
	s_nop 0
	global_load_lds_dwordx4 v2, s[98:99]
	s_add_i32 m0, s36, 0x2000
	s_add_i32 s36, s68, s33
	global_load_lds_dwordx4 v132, s[98:99]
	s_mov_b32 m0, s36
	s_nop 0
	global_load_lds_dwordx4 v136, s[98:99]
	s_add_i32 m0, s36, 0x2000
	s_nop 0
	global_load_lds_dwordx4 v0, s[98:99]
	s_waitcnt vmcnt(8)
	s_waitcnt lgkmcnt(0)
	s_barrier
	s_setprio 1
	s_waitcnt lgkmcnt(0)
	v_mfma_f32_16x16x32_bf16 v[64:67], v[144:147], v[184:187], v[64:67]
	v_mfma_f32_16x16x32_bf16 v[56:59], v[160:163], v[184:187], v[56:59]
	v_mfma_f32_16x16x32_bf16 v[48:51], v[144:147], v[192:195], v[48:51]
	v_mfma_f32_16x16x32_bf16 v[40:43], v[160:163], v[192:195], v[40:43]
	v_mfma_f32_16x16x32_bf16 v[32:35], v[144:147], v[212:215], v[32:35]
	v_mfma_f32_16x16x32_bf16 v[24:27], v[160:163], v[212:215], v[24:27]
	v_mfma_f32_16x16x32_bf16 v[16:19], v[144:147], v[220:223], v[16:19]
	v_mfma_f32_16x16x32_bf16 v[8:11], v[160:163], v[220:223], v[8:11]
	v_mfma_f32_16x16x32_bf16 v[64:67], v[156:159], v[188:191], v[64:67]
	v_mfma_f32_16x16x32_bf16 v[56:59], v[164:167], v[188:191], v[56:59]
	v_mfma_f32_16x16x32_bf16 v[48:51], v[156:159], v[196:199], v[48:51]
	v_mfma_f32_16x16x32_bf16 v[40:43], v[164:167], v[196:199], v[40:43]
	v_mfma_f32_16x16x32_bf16 v[32:35], v[156:159], v[216:219], v[32:35]
	v_mfma_f32_16x16x32_bf16 v[24:27], v[164:167], v[216:219], v[24:27]
	v_mfma_f32_16x16x32_bf16 v[16:19], v[156:159], v[224:227], v[16:19]
	v_mfma_f32_16x16x32_bf16 v[8:11], v[164:167], v[224:227], v[8:11]
	s_setprio 0
	s_setprio 1
	v_mfma_f32_16x16x32_bf16 v[60:63], v[168:171], v[184:187], v[60:63]
	v_mfma_f32_16x16x32_bf16 v[52:55], v[176:179], v[184:187], v[52:55]
	v_mfma_f32_16x16x32_bf16 v[44:47], v[168:171], v[192:195], v[44:47]
	v_mfma_f32_16x16x32_bf16 v[36:39], v[176:179], v[192:195], v[36:39]
	v_mfma_f32_16x16x32_bf16 v[28:31], v[168:171], v[212:215], v[28:31]
	v_mfma_f32_16x16x32_bf16 v[20:23], v[176:179], v[212:215], v[20:23]
	v_mfma_f32_16x16x32_bf16 v[12:15], v[168:171], v[220:223], v[12:15]
	v_mfma_f32_16x16x32_bf16 v[4:7], v[176:179], v[220:223], v[4:7]
	v_mfma_f32_16x16x32_bf16 v[60:63], v[172:175], v[188:191], v[60:63]
	v_mfma_f32_16x16x32_bf16 v[52:55], v[180:183], v[188:191], v[52:55]
	v_mfma_f32_16x16x32_bf16 v[44:47], v[172:175], v[196:199], v[44:47]
	v_mfma_f32_16x16x32_bf16 v[36:39], v[180:183], v[196:199], v[36:39]
	v_mfma_f32_16x16x32_bf16 v[28:31], v[172:175], v[216:219], v[28:31]
	v_mfma_f32_16x16x32_bf16 v[20:23], v[180:183], v[216:219], v[20:23]
	v_mfma_f32_16x16x32_bf16 v[12:15], v[172:175], v[224:227], v[12:15]
	v_mfma_f32_16x16x32_bf16 v[4:7], v[180:183], v[224:227], v[4:7]
	s_setprio 0
	s_barrier
	s_add_i32 s62, s62, 2
	s_add_u32 s46, s46, 0x100
	s_addc_u32 s47, s47, 0
	s_add_u32 s52, s52, 0x100
	s_addc_u32 s53, s53, 0
	s_cmp_gt_u32 s62, 13
	s_cbranch_scc1 .Lpeel_done_727
.LBB0_727:
	s_add_u32 s36, s46, 0xfffc0080
	s_addc_u32 s37, s47, -1
	s_add_i32 s63, 0, 0x10000
	s_cmp_eq_u32 s62, 12
	s_cselect_b32 s37, s11, s37
	s_cselect_b32 s36, s59, s36
	v_add_u32_e32 v148, s63, v151
	s_cselect_b32 s73, s9, s53
	s_cselect_b32 s72, s60, s52
	s_add_i32 s68, 0, 0x14000
	ds_read_b128 v[144:147], v148
	ds_read_b128 v[156:159], v148 offset:1024
	ds_read_b128 v[160:163], v148 offset:2048
	ds_read_b128 v[164:167], v148 offset:3072
	v_add_u32_e32 v148, s68, v151
	ds_read_b128 v[168:171], v148
	ds_read_b128 v[172:175], v148 offset:1024
	ds_read_b128 v[176:179], v148 offset:2048
	ds_read_b128 v[180:183], v148 offset:3072
	s_add_i32 m0, s43, 0xc000
	ds_read_b128 v[184:187], v154
	ds_read_b128 v[188:191], v154 offset:1024
	ds_read_b128 v[192:195], v154 offset:2048
	ds_read_b128 v[196:199], v154 offset:3072
	ds_read_b128 v[212:215], v154 offset:4096
	ds_read_b128 v[216:219], v154 offset:5120
	ds_read_b128 v[220:223], v154 offset:6144
	ds_read_b128 v[224:227], v154 offset:7168
	global_load_lds_dwordx4 v140, s[46:47]
	s_add_i32 m0, s43, 0xe000
	s_nop 0
	global_load_lds_dwordx4 v142, s[46:47]
	s_waitcnt vmcnt(8)
	s_waitcnt lgkmcnt(0)
	s_barrier
; #define PG8_STAGE(bufoff, gbase, voff) do { _Pragma("unroll") for (int _i = 0; _i < 2; ++_i) \
;         __builtin_amdgcn_global_load_lds((const unsigned*)((const char*)(gbase) + (voff)[_i]), (PG8_LAS unsigned*)(lds + (bufoff) + ldsw + _i * 8192), 16, 0, 0); } while (0)
; #define PG8_LDA(dst, b, h) do { _Pragma("unroll") for (int m = 0; m < 4; ++m) _Pragma("unroll") for (int k = 0; k < 2; ++k) dst[m][k] = *(const PG8_LAS bf16x8*)(lds + PG8_SA(b, h) + aoff + m * 2048 + k * 1024); } while (0)
; #define PG8_MMA(ai, bj, At, Bt) do { __builtin_amdgcn_s_setprio(1); _Pragma("unroll") for (int m = 0; m < 4; ++m) _Pragma("unroll") for (int n = 0; n < 2; ++n) _Pragma("unroll") for (int k = 0; k < 2; ++k) \
;         acc[ai][bj][m][n] = __builtin_amdgcn_mfma_f32_16x16x32_bf16(Bt[n][k], At[m][k], acc[ai][bj][m][n], 0, 0, 0); __builtin_amdgcn_s_setprio(0); } while (0)
; #define PG8_WAIT_V(n) asm volatile("s_waitcnt vmcnt(" #n ")" ::: "memory")
; #define PG8_WAIT_L(n) asm volatile("s_waitcnt lgkmcnt(" #n ")" ::: "memory")
; #define PG8_BAR __builtin_amdgcn_s_barrier()
; #define PG8_SCHED __builtin_amdgcn_sched_barrier(0)
; template <class Epi, class Sched, bool ALIGN_EPI = false, bool SP2 = false>
; __device__ __forceinline__ void gemm_phase(PG8_LAS unsigned char* lds, const Gemm g, const Sched& S, const Epi& E, const int tid) {
;     ...
;             PG8_WAIT_V(8); PG8_WAIT_L(0); PG8_BAR; PG8_MMA(0, 0, At, B0); PG8_MMA(0, 1, At, B1); PG8_BAR; PG8_SCHED;
;             PG8_LDA(At, 0, 1); PG8_STAGE(PG8_SB(0, 0), b2, voffB); PG8_STAGE(PG8_SB(0, 1), b2, voffB1); PG8_STAGE(PG8_SA(0, 0), a2, voffA);
;             PG8_WAIT_V(8); PG8_WAIT_L(0); PG8_BAR; PG8_MMA(1, 0, At, B0); PG8_MMA(1, 1, At, B1); PG8_BAR; PG8_SCHED;
	s_setprio 1
	s_waitcnt lgkmcnt(0)
	v_mfma_f32_16x16x32_bf16 v[128:131], v[144:147], v[184:187], v[128:131]
	v_mfma_f32_16x16x32_bf16 v[120:123], v[160:163], v[184:187], v[120:123]
	v_mfma_f32_16x16x32_bf16 v[112:115], v[144:147], v[192:195], v[112:115]
	v_mfma_f32_16x16x32_bf16 v[104:107], v[160:163], v[192:195], v[104:107]
	v_mfma_f32_16x16x32_bf16 v[96:99], v[144:147], v[212:215], v[96:99]
	v_mfma_f32_16x16x32_bf16 v[88:91], v[160:163], v[212:215], v[88:91]
	v_mfma_f32_16x16x32_bf16 v[80:83], v[144:147], v[220:223], v[80:83]
	v_mfma_f32_16x16x32_bf16 v[72:75], v[160:163], v[220:223], v[72:75]
	v_mfma_f32_16x16x32_bf16 v[128:131], v[156:159], v[188:191], v[128:131]
	v_mfma_f32_16x16x32_bf16 v[120:123], v[164:167], v[188:191], v[120:123]
	v_mfma_f32_16x16x32_bf16 v[112:115], v[156:159], v[196:199], v[112:115]
	v_mfma_f32_16x16x32_bf16 v[104:107], v[164:167], v[196:199], v[104:107]
	v_mfma_f32_16x16x32_bf16 v[96:99], v[156:159], v[216:219], v[96:99]
	v_mfma_f32_16x16x32_bf16 v[88:91], v[164:167], v[216:219], v[88:91]
	v_mfma_f32_16x16x32_bf16 v[80:83], v[156:159], v[224:227], v[80:83]
	v_mfma_f32_16x16x32_bf16 v[72:75], v[164:167], v[224:227], v[72:75]
	s_setprio 0
	s_setprio 1
	v_mfma_f32_16x16x32_bf16 v[124:127], v[168:171], v[184:187], v[124:127]
	v_mfma_f32_16x16x32_bf16 v[116:119], v[176:179], v[184:187], v[116:119]
	v_mfma_f32_16x16x32_bf16 v[108:111], v[168:171], v[192:195], v[108:111]
	v_mfma_f32_16x16x32_bf16 v[100:103], v[176:179], v[192:195], v[100:103]
	v_mfma_f32_16x16x32_bf16 v[92:95], v[168:171], v[212:215], v[92:95]
	v_mfma_f32_16x16x32_bf16 v[84:87], v[176:179], v[212:215], v[84:87]
	v_mfma_f32_16x16x32_bf16 v[76:79], v[168:171], v[220:223], v[76:79]
	v_mfma_f32_16x16x32_bf16 v[68:71], v[176:179], v[220:223], v[68:71]
	v_mfma_f32_16x16x32_bf16 v[124:127], v[172:175], v[188:191], v[124:127]
	v_mfma_f32_16x16x32_bf16 v[116:119], v[180:183], v[188:191], v[116:119]
	v_mfma_f32_16x16x32_bf16 v[108:111], v[172:175], v[196:199], v[108:111]
	v_mfma_f32_16x16x32_bf16 v[100:103], v[180:183], v[196:199], v[100:103]
	v_mfma_f32_16x16x32_bf16 v[92:95], v[172:175], v[216:219], v[92:95]
	v_mfma_f32_16x16x32_bf16 v[84:87], v[180:183], v[216:219], v[84:87]
	v_mfma_f32_16x16x32_bf16 v[76:79], v[172:175], v[224:227], v[76:79]
	v_mfma_f32_16x16x32_bf16 v[68:71], v[180:183], v[224:227], v[68:71]
	s_setprio 0
	s_barrier
	s_add_i32 s63, s63, s33
	s_mov_b32 m0, s63
	ds_read_b128 v[184:187], v154 offset:16384
	ds_read_b128 v[188:191], v154 offset:17408
	ds_read_b128 v[192:195], v154 offset:18432
	ds_read_b128 v[196:199], v154 offset:19456
	ds_read_b128 v[212:215], v154 offset:20480
	ds_read_b128 v[216:219], v154 offset:21504
	ds_read_b128 v[220:223], v154 offset:22528
	ds_read_b128 v[224:227], v154 offset:23552
	global_load_lds_dwordx4 v2, s[72:73]
	s_add_i32 m0, s63, 0x2000
	s_add_i32 s63, s68, s33
	global_load_lds_dwordx4 v132, s[72:73]
	s_mov_b32 m0, s63
	s_nop 0
	global_load_lds_dwordx4 v136, s[72:73]
	s_add_i32 m0, s63, 0x2000
	s_nop 0
	global_load_lds_dwordx4 v0, s[72:73]
	s_mov_b32 m0, s43
	s_nop 0
	global_load_lds_dwordx4 v138, s[36:37]
	s_mov_b32 m0, s45
	s_nop 0
	global_load_lds_dwordx4 v134, s[36:37]
	s_waitcnt vmcnt(8)
	s_waitcnt lgkmcnt(0)
	s_barrier
	s_setprio 1
	s_waitcnt lgkmcnt(0)
	v_mfma_f32_16x16x32_bf16 v[64:67], v[144:147], v[184:187], v[64:67]
	v_mfma_f32_16x16x32_bf16 v[56:59], v[160:163], v[184:187], v[56:59]
	v_mfma_f32_16x16x32_bf16 v[48:51], v[144:147], v[192:195], v[48:51]
	v_mfma_f32_16x16x32_bf16 v[40:43], v[160:163], v[192:195], v[40:43]
	v_mfma_f32_16x16x32_bf16 v[32:35], v[144:147], v[212:215], v[32:35]
	v_mfma_f32_16x16x32_bf16 v[24:27], v[160:163], v[212:215], v[24:27]
	v_mfma_f32_16x16x32_bf16 v[16:19], v[144:147], v[220:223], v[16:19]
	v_mfma_f32_16x16x32_bf16 v[8:11], v[160:163], v[220:223], v[8:11]
	v_mfma_f32_16x16x32_bf16 v[64:67], v[156:159], v[188:191], v[64:67]
	v_mfma_f32_16x16x32_bf16 v[56:59], v[164:167], v[188:191], v[56:59]
	v_mfma_f32_16x16x32_bf16 v[48:51], v[156:159], v[196:199], v[48:51]
	v_mfma_f32_16x16x32_bf16 v[40:43], v[164:167], v[196:199], v[40:43]
	v_mfma_f32_16x16x32_bf16 v[32:35], v[156:159], v[216:219], v[32:35]
	v_mfma_f32_16x16x32_bf16 v[24:27], v[164:167], v[216:219], v[24:27]
	v_mfma_f32_16x16x32_bf16 v[16:19], v[156:159], v[224:227], v[16:19]
	v_mfma_f32_16x16x32_bf16 v[8:11], v[164:167], v[224:227], v[8:11]
	s_setprio 0
	s_setprio 1
	v_mfma_f32_16x16x32_bf16 v[60:63], v[168:171], v[184:187], v[60:63]
	v_mfma_f32_16x16x32_bf16 v[52:55], v[176:179], v[184:187], v[52:55]
	v_mfma_f32_16x16x32_bf16 v[44:47], v[168:171], v[192:195], v[44:47]
	v_mfma_f32_16x16x32_bf16 v[36:39], v[176:179], v[192:195], v[36:39]
	v_mfma_f32_16x16x32_bf16 v[28:31], v[168:171], v[212:215], v[28:31]
	v_mfma_f32_16x16x32_bf16 v[20:23], v[176:179], v[212:215], v[20:23]
	v_mfma_f32_16x16x32_bf16 v[12:15], v[168:171], v[220:223], v[12:15]
	v_mfma_f32_16x16x32_bf16 v[4:7], v[176:179], v[220:223], v[4:7]
	v_mfma_f32_16x16x32_bf16 v[60:63], v[172:175], v[188:191], v[60:63]
	v_mfma_f32_16x16x32_bf16 v[52:55], v[180:183], v[188:191], v[52:55]
	v_mfma_f32_16x16x32_bf16 v[44:47], v[172:175], v[196:199], v[44:47]
	v_mfma_f32_16x16x32_bf16 v[36:39], v[180:183], v[196:199], v[36:39]
	v_mfma_f32_16x16x32_bf16 v[28:31], v[172:175], v[216:219], v[28:31]
	v_mfma_f32_16x16x32_bf16 v[20:23], v[180:183], v[216:219], v[20:23]
	v_mfma_f32_16x16x32_bf16 v[12:15], v[172:175], v[224:227], v[12:15]
	v_mfma_f32_16x16x32_bf16 v[4:7], v[180:183], v[224:227], v[4:7]
	s_setprio 0
	s_barrier
; #define PG8_STAGE(bufoff, gbase, voff) do { _Pragma("unroll") for (int _i = 0; _i < 2; ++_i) \
;         __builtin_amdgcn_global_load_lds((const unsigned*)((const char*)(gbase) + (voff)[_i]), (PG8_LAS unsigned*)(lds + (bufoff) + ldsw + _i * 8192), 16, 0, 0); } while (0)
; #define PG8_LDA(dst, b, h) do { _Pragma("unroll") for (int m = 0; m < 4; ++m) _Pragma("unroll") for (int k = 0; k < 2; ++k) dst[m][k] = *(const PG8_LAS bf16x8*)(lds + PG8_SA(b, h) + aoff + m * 2048 + k * 1024); } while (0)
; #define PG8_LDB(dst, b, h) do { _Pragma("unroll") for (int n = 0; n < 2; ++n) _Pragma("unroll") for (int k = 0; k < 2; ++k) dst[n][k] = *(const PG8_LAS bf16x8*)(lds + PG8_SB(b, h) + boff + n * 2048 + k * 1024); } while (0)
; #define PG8_MMA(ai, bj, At, Bt) do { __builtin_amdgcn_s_setprio(1); _Pragma("unroll") for (int m = 0; m < 4; ++m) _Pragma("unroll") for (int n = 0; n < 2; ++n) _Pragma("unroll") for (int k = 0; k < 2; ++k) \
;         acc[ai][bj][m][n] = __builtin_amdgcn_mfma_f32_16x16x32_bf16(Bt[n][k], At[m][k], acc[ai][bj][m][n], 0, 0, 0); __builtin_amdgcn_s_setprio(0); } while (0)
; #define PG8_WAIT_V(n) asm volatile("s_waitcnt vmcnt(" #n ")" ::: "memory")
; #define PG8_WAIT_L(n) asm volatile("s_waitcnt lgkmcnt(" #n ")" ::: "memory")
; #define PG8_BAR __builtin_amdgcn_s_barrier()
; #define PG8_SCHED __builtin_amdgcn_sched_barrier(0)
; template <class Epi, class Sched, bool ALIGN_EPI = false, bool SP2 = false>
; __device__ __forceinline__ void gemm_phase(PG8_LAS unsigned char* lds, const Gemm g, const Sched& S, const Epi& E, const int tid) {
;     ...
;             PG8_LDB(B0, 1, 0); PG8_LDB(B1, 1, 1); PG8_SCHED; PG8_LDA(At, 1, 0); PG8_STAGE(PG8_SA(0, 1), a2 + hstep, voffA);
;             PG8_WAIT_V(8); PG8_WAIT_L(0); PG8_BAR; PG8_MMA(0, 0, At, B0); PG8_MMA(0, 1, At, B1); PG8_BAR; PG8_SCHED;
;             PG8_LDA(At, 1, 1); PG8_STAGE(PG8_SB(1, 0), b3, voffB); PG8_STAGE(PG8_SB(1, 1), b3, voffB1); PG8_STAGE(PG8_SA(1, 0), a3, voffA);
;             PG8_WAIT_V(8); PG8_WAIT_L(0); PG8_BAR; PG8_MMA(1, 0, At, B0); PG8_MMA(1, 1, At, B1); PG8_BAR; PG8_SCHED;
	s_add_i32 s63, 0, 0x18000
	v_add_u32_e32 v155, s63, v151
	s_add_i32 s68, 0, 0x1c000
	ds_read_b128 v[144:147], v155
	ds_read_b128 v[156:159], v155 offset:1024
	ds_read_b128 v[160:163], v155 offset:2048
	ds_read_b128 v[164:167], v155 offset:3072
	v_add_u32_e32 v155, s68, v151
	ds_read_b128 v[168:171], v155
	ds_read_b128 v[172:175], v155 offset:1024
	ds_read_b128 v[176:179], v155 offset:2048
	ds_read_b128 v[180:183], v155 offset:3072
	s_add_u32 s36, s36, 0x40000
	s_addc_u32 s37, s37, 0
	s_mov_b32 m0, s48
	ds_read_b128 v[184:187], v154 offset:32768
	ds_read_b128 v[188:191], v154 offset:33792
	ds_read_b128 v[192:195], v154 offset:34816
	ds_read_b128 v[196:199], v154 offset:35840
	ds_read_b128 v[212:215], v154 offset:36864
	ds_read_b128 v[216:219], v154 offset:37888
	ds_read_b128 v[220:223], v154 offset:38912
	ds_read_b128 v[224:227], v154 offset:39936
	global_load_lds_dwordx4 v138, s[36:37]
	s_mov_b32 m0, s49
	s_nop 0
	global_load_lds_dwordx4 v134, s[36:37]
	s_waitcnt vmcnt(8)
	s_waitcnt lgkmcnt(0)
	s_barrier
	s_setprio 1
	s_waitcnt lgkmcnt(0)
	v_mfma_f32_16x16x32_bf16 v[128:131], v[144:147], v[184:187], v[128:131]
	v_mfma_f32_16x16x32_bf16 v[120:123], v[160:163], v[184:187], v[120:123]
	v_mfma_f32_16x16x32_bf16 v[112:115], v[144:147], v[192:195], v[112:115]
	v_mfma_f32_16x16x32_bf16 v[104:107], v[160:163], v[192:195], v[104:107]
	v_mfma_f32_16x16x32_bf16 v[96:99], v[144:147], v[212:215], v[96:99]
	v_mfma_f32_16x16x32_bf16 v[88:91], v[160:163], v[212:215], v[88:91]
	v_mfma_f32_16x16x32_bf16 v[80:83], v[144:147], v[220:223], v[80:83]
	v_mfma_f32_16x16x32_bf16 v[72:75], v[160:163], v[220:223], v[72:75]
	v_mfma_f32_16x16x32_bf16 v[128:131], v[156:159], v[188:191], v[128:131]
	v_mfma_f32_16x16x32_bf16 v[120:123], v[164:167], v[188:191], v[120:123]
	v_mfma_f32_16x16x32_bf16 v[112:115], v[156:159], v[196:199], v[112:115]
	v_mfma_f32_16x16x32_bf16 v[104:107], v[164:167], v[196:199], v[104:107]
	v_mfma_f32_16x16x32_bf16 v[96:99], v[156:159], v[216:219], v[96:99]
	v_mfma_f32_16x16x32_bf16 v[88:91], v[164:167], v[216:219], v[88:91]
	v_mfma_f32_16x16x32_bf16 v[80:83], v[156:159], v[224:227], v[80:83]
	v_mfma_f32_16x16x32_bf16 v[72:75], v[164:167], v[224:227], v[72:75]
	s_setprio 0
	s_setprio 1
	v_mfma_f32_16x16x32_bf16 v[124:127], v[168:171], v[184:187], v[124:127]
	v_mfma_f32_16x16x32_bf16 v[116:119], v[176:179], v[184:187], v[116:119]
	v_mfma_f32_16x16x32_bf16 v[108:111], v[168:171], v[192:195], v[108:111]
	v_mfma_f32_16x16x32_bf16 v[100:103], v[176:179], v[192:195], v[100:103]
	v_mfma_f32_16x16x32_bf16 v[92:95], v[168:171], v[212:215], v[92:95]
	v_mfma_f32_16x16x32_bf16 v[84:87], v[176:179], v[212:215], v[84:87]
	v_mfma_f32_16x16x32_bf16 v[76:79], v[168:171], v[220:223], v[76:79]
	v_mfma_f32_16x16x32_bf16 v[68:71], v[176:179], v[220:223], v[68:71]
	v_mfma_f32_16x16x32_bf16 v[124:127], v[172:175], v[188:191], v[124:127]
	v_mfma_f32_16x16x32_bf16 v[116:119], v[180:183], v[188:191], v[116:119]
	v_mfma_f32_16x16x32_bf16 v[108:111], v[172:175], v[196:199], v[108:111]
	v_mfma_f32_16x16x32_bf16 v[100:103], v[180:183], v[196:199], v[100:103]
	v_mfma_f32_16x16x32_bf16 v[92:95], v[172:175], v[216:219], v[92:95]
	v_mfma_f32_16x16x32_bf16 v[84:87], v[180:183], v[216:219], v[84:87]
	v_mfma_f32_16x16x32_bf16 v[76:79], v[172:175], v[224:227], v[76:79]
	v_mfma_f32_16x16x32_bf16 v[68:71], v[180:183], v[224:227], v[68:71]
	s_setprio 0
	s_barrier
	s_add_u32 s98, s36, s66
	s_addc_u32 s99, s37, s67
	s_sub_u32 s98, s98, 0x40000
	s_subb_u32 s99, s99, 0
	s_mov_b32 m0, s50
	ds_read_b128 v[184:187], v154 offset:49152
	ds_read_b128 v[188:191], v154 offset:50176
	ds_read_b128 v[192:195], v154 offset:51200
	ds_read_b128 v[196:199], v154 offset:52224
	ds_read_b128 v[212:215], v154 offset:53248
	ds_read_b128 v[216:219], v154 offset:54272
	ds_read_b128 v[220:223], v154 offset:55296
	ds_read_b128 v[224:227], v154 offset:56320
	global_load_lds_dwordx4 v138, s[98:99]
	s_mov_b32 m0, s51
	s_nop 0
	global_load_lds_dwordx4 v134, s[98:99]
	s_add_u32 s98, s72, s66
	s_addc_u32 s99, s73, s67
	s_add_i32 s36, s63, s33
	s_mov_b32 m0, s36
	s_nop 0
	global_load_lds_dwordx4 v2, s[98:99]
	s_add_i32 m0, s36, 0x2000
	s_add_i32 s36, s68, s33
	global_load_lds_dwordx4 v132, s[98:99]
	s_mov_b32 m0, s36
	s_nop 0
	global_load_lds_dwordx4 v136, s[98:99]
	s_add_i32 m0, s36, 0x2000
	s_nop 0
	global_load_lds_dwordx4 v0, s[98:99]
	s_waitcnt vmcnt(8)
	s_waitcnt lgkmcnt(0)
	s_barrier
	s_setprio 1
	s_waitcnt lgkmcnt(0)
	v_mfma_f32_16x16x32_bf16 v[64:67], v[144:147], v[184:187], v[64:67]
	v_mfma_f32_16x16x32_bf16 v[56:59], v[160:163], v[184:187], v[56:59]
	v_mfma_f32_16x16x32_bf16 v[48:51], v[144:147], v[192:195], v[48:51]
	v_mfma_f32_16x16x32_bf16 v[40:43], v[160:163], v[192:195], v[40:43]
	v_mfma_f32_16x16x32_bf16 v[32:35], v[144:147], v[212:215], v[32:35]
	v_mfma_f32_16x16x32_bf16 v[24:27], v[160:163], v[212:215], v[24:27]
	v_mfma_f32_16x16x32_bf16 v[16:19], v[144:147], v[220:223], v[16:19]
	v_mfma_f32_16x16x32_bf16 v[8:11], v[160:163], v[220:223], v[8:11]
	v_mfma_f32_16x16x32_bf16 v[64:67], v[156:159], v[188:191], v[64:67]
	v_mfma_f32_16x16x32_bf16 v[56:59], v[164:167], v[188:191], v[56:59]
	v_mfma_f32_16x16x32_bf16 v[48:51], v[156:159], v[196:199], v[48:51]
	v_mfma_f32_16x16x32_bf16 v[40:43], v[164:167], v[196:199], v[40:43]
	v_mfma_f32_16x16x32_bf16 v[32:35], v[156:159], v[216:219], v[32:35]
	v_mfma_f32_16x16x32_bf16 v[24:27], v[164:167], v[216:219], v[24:27]
	v_mfma_f32_16x16x32_bf16 v[16:19], v[156:159], v[224:227], v[16:19]
	v_mfma_f32_16x16x32_bf16 v[8:11], v[164:167], v[224:227], v[8:11]
	s_setprio 0
	s_setprio 1
	v_mfma_f32_16x16x32_bf16 v[60:63], v[168:171], v[184:187], v[60:63]
	v_mfma_f32_16x16x32_bf16 v[52:55], v[176:179], v[184:187], v[52:55]
	v_mfma_f32_16x16x32_bf16 v[44:47], v[168:171], v[192:195], v[44:47]
	v_mfma_f32_16x16x32_bf16 v[36:39], v[176:179], v[192:195], v[36:39]
	v_mfma_f32_16x16x32_bf16 v[28:31], v[168:171], v[212:215], v[28:31]
	v_mfma_f32_16x16x32_bf16 v[20:23], v[176:179], v[212:215], v[20:23]
	v_mfma_f32_16x16x32_bf16 v[12:15], v[168:171], v[220:223], v[12:15]
	v_mfma_f32_16x16x32_bf16 v[4:7], v[176:179], v[220:223], v[4:7]
	v_mfma_f32_16x16x32_bf16 v[60:63], v[172:175], v[188:191], v[60:63]
	v_mfma_f32_16x16x32_bf16 v[52:55], v[180:183], v[188:191], v[52:55]
	v_mfma_f32_16x16x32_bf16 v[44:47], v[172:175], v[196:199], v[44:47]
	v_mfma_f32_16x16x32_bf16 v[36:39], v[180:183], v[196:199], v[36:39]
	v_mfma_f32_16x16x32_bf16 v[28:31], v[172:175], v[216:219], v[28:31]
	v_mfma_f32_16x16x32_bf16 v[20:23], v[180:183], v[216:219], v[20:23]
	v_mfma_f32_16x16x32_bf16 v[12:15], v[172:175], v[224:227], v[12:15]
	v_mfma_f32_16x16x32_bf16 v[4:7], v[180:183], v[224:227], v[4:7]
	s_setprio 0
	s_barrier
	s_add_i32 s62, s62, 2
	s_add_u32 s46, s46, 0x100
	s_addc_u32 s47, s47, 0
	s_add_u32 s52, s52, 0x100
	s_addc_u32 s53, s53, 0
	s_cmp_gt_u32 s62, 13
	s_cbranch_scc0 .LBB0_727
